# baseline (speedup 1.0000x reference)
.Lh_no_out:
	s_cmp_eq_u32 s17, 0
	s_cselect_b32 s4, s4, s6
	s_cselect_b32 s5, s5, s7
	s_add_u32 s24, s8, s22
	s_addc_u32 s25, s9, 0
	s_add_u32 s4, s4, s21
	s_addc_u32 s5, s5, 0
	global_load_dwordx4 v[14:17], v18, s[24:25] nt
	global_load_dwordx4 v[2:5], v18, s[4:5] nt
	s_add_u32 s6, s4, 0x40000
	s_addc_u32 s7, s5, 0
	s_add_u32 s8, s4, 0x80000
	s_addc_u32 s9, s5, 0
	s_barrier
	global_load_dwordx4 v[6:9], v18, s[6:7] nt
	s_barrier
	global_load_dwordx4 v[10:13], v18, s[8:9] nt
	s_mul_i32 s46, s3, 0xc00
	s_add_u32 s46, s46, 0x8420
	v_lshl_add_u32 v26, v1, 2, s46
	v_and_b32_e32 v38, 15, v0
	s_mul_i32 s58, s17, 0x4200
	s_add_u32 s58, s58, 0x1e0
	v_lshl_add_u32 v38, v38, 2, s58
	v_add_u32_e32 v39, 0x1600, v38
	v_add_u32_e32 v40, 0x2c00, v38
	v_mov_b32_e32 v41, 0x41fc0000
	v_mov_b32_e32 v50, 0x3ebc5ab2
	v_mov_b32_e32 v51, 0x3ebc5ab2
	v_mov_b32_e32 v52, 0x3fb8aa3b
	v_mov_b32_e32 v53, 0x3fb8aa3b
	v_mov_b32_e32 v54, 0xbf38aa3b
	v_mov_b32_e32 v55, 0xbf38aa3b
	s_mov_b32 s48, 0x3f940000
	s_mov_b32 s51, 0x3fb8aa3b
	s_mov_b32 s42, 0
	s_mov_b32 s43, 0
	s_mov_b32 s44, 0x7fffffff
	s_mov_b32 s45, 0x7fffffff
	s_mov_b32 s47, 0
	s_mul_i32 s58, s3, 0x1600
	s_add_u32 s58, s58, 0x320
	v_lshl_add_u32 v44, v1, 6, s58
	v_bfe_u32 v45, v1, 2, 2
	v_lshlrev_b32_e32 v45, 4, v45
	v_xor_b32_e32 v46, 16, v45
	v_xor_b32_e32 v47, 32, v45
	v_xor_b32_e32 v48, 48, v45
	v_add_u32_e32 v45, v44, v45
	v_add_u32_e32 v46, v44, v46
	v_add_u32_e32 v47, v44, v47
	v_add_u32_e32 v48, v44, v48
	s_mul_i32 s58, s2, 0x600
	s_lshl_b32 s59, s3, 8
	s_add_u32 s58, s58, s59
	s_add_u32 s10, s10, s58
	s_addc_u32 s11, s11, 0
	v_lshlrev_b32_e32 v49, 2, v1
	s_lshl_b32 s58, s2, 2
	s_add_u32 s12, s12, s58
	s_addc_u32 s13, s13, 0
	s_waitcnt vmcnt(3)
	v_cmp_lt_f32_e64 s[26:27], 0.5, v14
	v_cmp_lt_f32_e64 s[28:29], 0.5, v15
	v_cmp_lt_f32_e64 s[30:31], 0.5, v16
	v_cmp_lt_f32_e64 s[32:33], 0.5, v17
	s_cmp_lg_u32 s17, 0
	s_cbranch_scc1 .Lh_no_cnt
	s_bcnt1_i32_b64 s54, s[26:27]
	s_bcnt1_i32_b64 s55, s[28:29]
	s_bcnt1_i32_b64 s56, s[30:31]
	s_bcnt1_i32_b64 s57, s[32:33]
	s_add_i32 s54, s54, s55
	s_add_i32 s56, s56, s57
	s_add_i32 s54, s54, s56
	s_lshl_b32 s55, s16, 2
	v_mov_b32_e32 v36, s55
	v_mov_b32_e32 v37, s54
	s_mov_b64 exec, 1
	ds_write_b32 v36, v37
	s_mov_b64 exec, -1

.Lh_loop_body:
	v_fmamk_f32 v27, v24, 0x42000000, v41
	v_add_u32_e32 v26, 0x100, v26
	ds_read_b32 v24, v26
	s_sub_i32 s49, s44, s43
	s_sub_i32 s50, s45, s43
	s_add_i32 s43, s43, 64
	v_rndne_f32_e32 v28, v27
	v_cmp_le_i32_e32 vcc, s49, v1
	v_cmp_le_i32_e64 s[52:53], s50, v1
	v_sub_f32_e32 v29, v27, v28
	v_cvt_i32_f32_e32 v30, v28
	v_cndmask_b32_e32 v36, v38, v39, vcc
	v_mul_f32_e32 v37, 0xbf38aa3b, v29
	v_cndmask_b32_e64 v36, v36, v40, s[52:53]
	v_pk_fma_f32 v[32:33], v[28:29], v[52:53], v[54:55] op_sel:[1,0,0] op_sel_hi:[1,1,1] neg_hi:[1,0,0]
	v_fmaak_f32 v31, v29, v37, 0x41a00000
	v_lshl_add_u32 v30, v30, 6, v36
	v_exp_f32_e32 v31, v31
	v_exp_f32_e32 v32, v32
	v_exp_f32_e32 v33, v33
	v_cvt_rpi_i32_f32_e32 v36, v31
	ds_add_u32 v30, v36 offset:320
	v_pk_mul_f32 v[34:35], v[32:33], v[30:31] op_sel:[0,1] op_sel_hi:[1,1]
	v_pk_mul_f32 v[32:33], v[32:33], v[50:51]
	v_cvt_rpi_i32_f32_e32 v36, v34
	v_cvt_rpi_i32_f32_e32 v37, v35
	ds_add_u32 v30, v36 offset:384
	ds_add_u32 v30, v37 offset:256
	v_pk_mul_f32 v[34:35], v[32:33], v[34:35]
	v_pk_mul_f32 v[32:33], v[32:33], v[50:51]
	v_cvt_rpi_i32_f32_e32 v36, v34
	v_cvt_rpi_i32_f32_e32 v37, v35
	ds_add_u32 v30, v36 offset:448
	ds_add_u32 v30, v37 offset:192
	v_pk_mul_f32 v[34:35], v[32:33], v[34:35]
	v_pk_mul_f32 v[32:33], v[32:33], v[50:51]
	v_cvt_rpi_i32_f32_e32 v36, v34
	v_cvt_rpi_i32_f32_e32 v37, v35
	ds_add_u32 v30, v36 offset:512
	ds_add_u32 v30, v37 offset:128
	v_pk_mul_f32 v[34:35], v[32:33], v[34:35]
	v_pk_mul_f32 v[32:33], v[32:33], v[50:51]
	v_cvt_rpi_i32_f32_e32 v36, v34
	v_cvt_rpi_i32_f32_e32 v37, v35
	ds_add_u32 v30, v36 offset:576
	ds_add_u32 v30, v37 offset:64
	v_pk_mul_f32 v[34:35], v[32:33], v[34:35]
	v_cvt_rpi_i32_f32_e32 v36, v34
	v_cvt_rpi_i32_f32_e32 v37, v35
	ds_add_u32 v30, v36 offset:640
	ds_add_u32 v30, v37
	s_sub_i32 s59, s42, s43
	s_cmp_ge_i32 s59, 64
	s_waitcnt lgkmcnt(11)
	s_cbranch_scc1 .Lh_loop_body

	.amdhsa_kernel _Z6k_histPKfS0_S0_PfPiS1_
		.amdhsa_group_segment_fixed_size 32
		.amdhsa_private_segment_fixed_size 0
		.amdhsa_kernarg_size 48
		.amdhsa_user_sgpr_count 2
		.amdhsa_user_sgpr_dispatch_ptr 0
		.amdhsa_user_sgpr_queue_ptr 0
		.amdhsa_user_sgpr_kernarg_segment_ptr 1
		.amdhsa_user_sgpr_dispatch_id 0
		.amdhsa_user_sgpr_kernarg_preload_length 0
		.amdhsa_user_sgpr_kernarg_preload_offset 0
		.amdhsa_user_sgpr_private_segment_size 0
		.amdhsa_uses_dynamic_stack 0
		.amdhsa_enable_private_segment 0
		.amdhsa_system_sgpr_workgroup_id_x 1
		.amdhsa_system_sgpr_workgroup_id_y 0
		.amdhsa_system_sgpr_workgroup_id_z 0
		.amdhsa_system_sgpr_workgroup_info 0
		.amdhsa_system_vgpr_workitem_id 0
		.amdhsa_next_free_vgpr 56
		.amdhsa_next_free_sgpr 60
		.amdhsa_accum_offset 56
		.amdhsa_reserve_vcc 1
		.amdhsa_float_round_mode_32 0
		.amdhsa_float_round_mode_16_64 0
		.amdhsa_float_denorm_mode_32 3
		.amdhsa_float_denorm_mode_16_64 3
		.amdhsa_dx10_clamp 1
		.amdhsa_ieee_mode 1
		.amdhsa_fp16_overflow 0
		.amdhsa_tg_split 0
		.amdhsa_exception_fp_ieee_invalid_op 0
		.amdhsa_exception_fp_denorm_src 0
		.amdhsa_exception_fp_ieee_div_zero 0
		.amdhsa_exception_fp_ieee_overflow 0
		.amdhsa_exception_fp_ieee_underflow 0
		.amdhsa_exception_fp_ieee_inexact 0
		.amdhsa_exception_int_div_zero 0
	.end_amdhsa_kernel

.Lfunc_end0:
	.size	_Z6k_histPKfS0_S0_PfPiS1_, .Lfunc_end0-_Z6k_histPKfS0_S0_PfPiS1_
	.set _Z6k_histPKfS0_S0_PfPiS1_.num_vgpr, 56
	.set _Z6k_histPKfS0_S0_PfPiS1_.num_agpr, 0
	.set _Z6k_histPKfS0_S0_PfPiS1_.numbered_sgpr, 60
	.set _Z6k_histPKfS0_S0_PfPiS1_.num_named_barrier, 0
	.set _Z6k_histPKfS0_S0_PfPiS1_.private_seg_size, 0
	.set _Z6k_histPKfS0_S0_PfPiS1_.uses_vcc, 1
	.set _Z6k_histPKfS0_S0_PfPiS1_.uses_flat_scratch, 0
	.set _Z6k_histPKfS0_S0_PfPiS1_.has_dyn_sized_stack, 0
	.set _Z6k_histPKfS0_S0_PfPiS1_.has_recursion, 0
	.set _Z6k_histPKfS0_S0_PfPiS1_.has_indirect_call, 0

amdhsa.kernels:
  - .agpr_count:     0
    .args:
      - .actual_access:  read_only
        .address_space:  global
        .offset:         0
        .size:           8
        .value_kind:     global_buffer
      - .actual_access:  read_only
        .address_space:  global
        .offset:         8
        .size:           8
        .value_kind:     global_buffer
      - .actual_access:  read_only
        .address_space:  global
        .offset:         16
        .size:           8
        .value_kind:     global_buffer
      - .actual_access:  write_only
        .address_space:  global
        .offset:         24
        .size:           8
        .value_kind:     global_buffer
      - .actual_access:  write_only
        .address_space:  global
        .offset:         32
        .size:           8
        .value_kind:     global_buffer
      - .actual_access:  write_only
        .address_space:  global
        .offset:         40
        .size:           8
        .value_kind:     global_buffer
    .group_segment_fixed_size: 32
    .kernarg_segment_align: 8
    .kernarg_segment_size: 48
    .language:       OpenCL C
    .language_version:
      - 2
      - 0
    .max_flat_workgroup_size: 1024
    .name:           _Z6k_histPKfS0_S0_PfPiS1_
    .private_segment_fixed_size: 0
    .sgpr_count:     66
    .sgpr_spill_count: 0
    .symbol:         _Z6k_histPKfS0_S0_PfPiS1_.kd
    .uniform_work_group_size: 1
    .uses_dynamic_stack: false
    .vgpr_count:     56
    .vgpr_spill_count: 0
    .wavefront_size: 64
  - .agpr_count:     0
    .args:
      - .actual_access:  read_only
        .address_space:  global
        .offset:         0
        .size:           8
        .value_kind:     global_buffer
      - .actual_access:  read_only
        .address_space:  global
        .offset:         8
        .size:           8
        .value_kind:     global_buffer
      - .address_space:  global
        .offset:         16
        .size:           8
        .value_kind:     global_buffer
    .group_segment_fixed_size: 2080
    .kernarg_segment_align: 8
    .kernarg_segment_size: 24
    .language:       OpenCL C
    .language_version:
      - 2
      - 0
    .max_flat_workgroup_size: 256
    .name:           _Z7k_finalPKfPKiPf
    .private_segment_fixed_size: 0
    .sgpr_count:     34
    .sgpr_spill_count: 0
    .symbol:         _Z7k_finalPKfPKiPf.kd
    .uniform_work_group_size: 1
    .uses_dynamic_stack: false
    .vgpr_count:     36
    .vgpr_spill_count: 0
    .wavefront_size: 64
